# score loop B: K tile LDS write moved mid-tile + extra workgroup barrier there (on top of pk_final)
# baseline (speedup 1.0000x reference)
.Ls1_b:
	s_nop 11
	v_max_i32_e32 v14, 0, v26
	v_max_i32_e32 v15, 0, v27
	v_max_i32_e32 v16, 0, v34
	v_max_i32_e32 v17, 0, v35
	v_max_i32_e32 v34, 0, v28
	v_max_i32_e32 v35, 0, v29
	v_fma_f32 v168, v106, v14, 0
	v_fma_f32 v169, v107, v15, 0
	v_fma_f32 v170, v114, v16, 0
	v_fma_f32 v171, v115, v17, 0
	v_mfma_f32_32x32x16_bf16 v[14:29], v[66:69], v[2:5], 0
	v_max_i32_e32 v2, 0, v36
	v_max_i32_e32 v3, 0, v37
	v_max_i32_e32 v4, 0, v30
	v_max_i32_e32 v5, 0, v31
	v_max_i32_e32 v30, 0, v38
	v_max_i32_e32 v31, 0, v39
	v_fma_f32 v34, v108, v34, v168
	v_fma_f32 v35, v109, v35, v169
	v_fma_f32 v2, v116, v2, v170
	v_fma_f32 v3, v117, v3, v171
	v_mfma_f32_32x32x16_bf16 v[14:29], v[70:73], v[6:9], v[14:29]
	v_fma_f32 v4, v110, v4, v34
	v_fma_f32 v5, v111, v5, v35
	v_fma_f32 v2, v118, v30, v2
	v_fma_f32 v3, v119, v31, v3
	v_max_i32_e32 v6, 0, v32
	v_max_i32_e32 v7, 0, v33
	v_max_i32_e32 v8, 0, v40
	v_max_i32_e32 v9, 0, v41
	v_fma_f32 v4, v112, v6, v4
	v_fma_f32 v5, v113, v7, v5
	v_fma_f32 v2, v120, v8, v2
	v_fma_f32 v3, v121, v9, v3
	v_mfma_f32_32x32x16_bf16 v[14:29], v[74:77], v[10:13], v[14:29]
	v_add_f32_e32 v4, v4, v5
	v_add_f32_e32 v2, v2, v3
	ds_read_b128 v[168:171], v172 offset:96
	s_nop 0
	v_permlane32_swap_b32_e32 v4, v2
	v_add_f32_e32 v2, v4, v2
	ds_write_b32 v173, v2 offset:36864
	v_mfma_f32_32x32x16_bf16 v[14:29], v[78:81], v[42:45], v[14:29]
	s_nop 11
	v_max_i32_e32 v2, 0, v14
	v_max_i32_e32 v3, 0, v15
	v_max_i32_e32 v4, 0, v22
	v_max_i32_e32 v5, 0, v23
	v_max_i32_e32 v22, 0, v16
	v_max_i32_e32 v23, 0, v17
	v_fma_f32 v30, v122, v2, 0
	v_fma_f32 v31, v123, v3, 0
	v_fma_f32 v32, v130, v4, 0
	v_fma_f32 v33, v131, v5, 0
	s_waitcnt lgkmcnt(4)
	v_mfma_f32_32x32x16_bf16 v[2:17], v[50:53], v[46:49], 0
	v_max_i32_e32 v24, 0, v24
	v_max_i32_e32 v25, 0, v25
	v_max_i32_e32 v18, 0, v18
	v_max_i32_e32 v19, 0, v19
	v_max_i32_e32 v26, 0, v26
	v_max_i32_e32 v27, 0, v27
	v_fma_f32 v22, v124, v22, v30
	v_fma_f32 v23, v125, v23, v31
	v_fma_f32 v24, v132, v24, v32
	v_fma_f32 v25, v133, v25, v33
	s_waitcnt lgkmcnt(3)
	v_mfma_f32_32x32x16_bf16 v[2:17], v[54:57], v[160:163], v[2:17]
	v_fma_f32 v18, v126, v18, v22
	v_fma_f32 v19, v127, v19, v23
	v_fma_f32 v22, v134, v26, v24
	v_fma_f32 v23, v135, v27, v25
	v_max_i32_e32 v20, 0, v20
	v_max_i32_e32 v21, 0, v21
	v_max_i32_e32 v24, 0, v28
	v_max_i32_e32 v25, 0, v29
	v_fma_f32 v18, v128, v20, v18
	v_fma_f32 v19, v129, v21, v19
	v_fma_f32 v20, v136, v24, v22
	v_fma_f32 v21, v137, v25, v23
	s_waitcnt lgkmcnt(2)
	v_mfma_f32_32x32x16_bf16 v[2:17], v[58:61], v[164:167], v[2:17]
	v_add_f32_e32 v18, v18, v19
	v_add_f32_e32 v20, v20, v21
	s_nop 1
	v_permlane32_swap_b32_e32 v18, v20
	v_add_f32_e32 v18, v18, v20
	s_waitcnt lgkmcnt(1)
	v_mfma_f32_32x32x16_bf16 v[2:17], v[62:65], v[168:171], v[2:17]
	ds_write_b32 v173, v18 offset:37920
	ds_read_b128 v[172:175], v159 offset:9216
	s_nop 9
	v_max_i32_e32 v2, 0, v2
	v_max_i32_e32 v3, 0, v3
	v_max_i32_e32 v10, 0, v10
	v_max_i32_e32 v11, 0, v11
	v_max_i32_e32 v4, 0, v4
	v_max_i32_e32 v5, 0, v5
	v_fma_f32 v2, v106, v2, 0
	v_fma_f32 v3, v107, v3, 0
	v_fma_f32 v10, v114, v10, 0
	v_fma_f32 v11, v115, v11, 0
	v_mfma_f32_32x32x16_bf16 v[30:45], v[66:69], v[46:49], 0
	v_max_i32_e32 v12, 0, v12
	v_max_i32_e32 v13, 0, v13
	v_max_i32_e32 v6, 0, v6
	v_max_i32_e32 v7, 0, v7
	v_max_i32_e32 v14, 0, v14
	v_max_i32_e32 v15, 0, v15
	v_fma_f32 v2, v108, v4, v2
	v_fma_f32 v3, v109, v5, v3
	v_fma_f32 v4, v116, v12, v10
	v_fma_f32 v5, v117, v13, v11
	v_mfma_f32_32x32x16_bf16 v[30:45], v[70:73], v[160:163], v[30:45]
	v_fma_f32 v2, v110, v6, v2
	v_fma_f32 v3, v111, v7, v3
	v_fma_f32 v4, v118, v14, v4
	v_fma_f32 v5, v119, v15, v5
	v_max_i32_e32 v6, 0, v8
	v_max_i32_e32 v7, 0, v9
	v_max_i32_e32 v8, 0, v16
	v_max_i32_e32 v9, 0, v17
	v_fma_f32 v10, v112, v6, v2
	v_fma_f32 v11, v113, v7, v3
	v_fma_f32 v12, v120, v8, v4
	v_fma_f32 v13, v121, v9, v5
	v_mfma_f32_32x32x16_bf16 v[30:45], v[74:77], v[164:167], v[30:45]
	v_add_f32_e32 v10, v10, v11
	v_add_f32_e32 v12, v12, v13
	ds_read_b128 v[2:5], v159 offset:9248
	s_nop 0
	v_permlane32_swap_b32_e32 v10, v12
	v_add_f32_e32 v164, v10, v12
	ds_read_b128 v[6:9], v159 offset:9280
	v_mfma_f32_32x32x16_bf16 v[30:45], v[78:81], v[168:171], v[30:45]
	ds_read_b128 v[160:163], v159 offset:9312
	ds_write_b32 v180, v164 offset:36992
	s_nop 9
	v_max_i32_e32 v10, 0, v30
	v_max_i32_e32 v11, 0, v31
	v_max_i32_e32 v12, 0, v38
	v_max_i32_e32 v13, 0, v39
	v_max_i32_e32 v14, 0, v32
	v_max_i32_e32 v15, 0, v33
	v_fma_f32 v10, v122, v10, 0
	v_fma_f32 v11, v123, v11, 0
	v_fma_f32 v12, v130, v12, 0
	v_fma_f32 v13, v131, v13, 0
	s_waitcnt lgkmcnt(4)
	v_mfma_f32_32x32x16_bf16 v[18:33], v[50:53], v[172:175], 0
	v_max_i32_e32 v16, 0, v40
	v_max_i32_e32 v17, 0, v41
	v_max_i32_e32 v34, 0, v34
	v_max_i32_e32 v35, 0, v35
	v_max_i32_e32 v38, 0, v42
	v_max_i32_e32 v39, 0, v43
	v_fma_f32 v10, v124, v14, v10
	v_fma_f32 v11, v125, v15, v11
	v_fma_f32 v12, v132, v16, v12
	v_fma_f32 v13, v133, v17, v13
	s_waitcnt lgkmcnt(3)
	v_mfma_f32_32x32x16_bf16 v[18:33], v[54:57], v[2:5], v[18:33]
	v_fma_f32 v10, v126, v34, v10
	v_fma_f32 v11, v127, v35, v11
	v_fma_f32 v12, v134, v38, v12
	v_fma_f32 v13, v135, v39, v13
	v_max_i32_e32 v14, 0, v36
	v_max_i32_e32 v15, 0, v37
	v_max_i32_e32 v16, 0, v44
	v_max_i32_e32 v17, 0, v45
	v_fma_f32 v10, v128, v14, v10
	v_fma_f32 v11, v129, v15, v11
	v_fma_f32 v12, v136, v16, v12
	v_fma_f32 v13, v137, v17, v13
	s_waitcnt lgkmcnt(2)
	v_mfma_f32_32x32x16_bf16 v[18:33], v[58:61], v[6:9], v[18:33]
	v_add_f32_e32 v10, v10, v11
	v_add_f32_e32 v12, v12, v13
	v_add3_u32 v11, s1, v154, v102
	s_nop 0
	v_permlane32_swap_b32_e32 v10, v12
	v_add_f32_e32 v10, v10, v12
	ds_write_b32 v180, v10 offset:38048
	s_waitcnt lgkmcnt(2)
	v_mfma_f32_32x32x16_bf16 v[18:33], v[62:65], v[160:163], v[18:33]
	ds_read_b128 v[164:167], v11
	ds_read_b128 v[168:171], v11 offset:32
	ds_read_b128 v[176:179], v11 offset:96
	s_nop 8
	v_max_i32_e32 v18, 0, v18
	v_max_i32_e32 v19, 0, v19
	v_max_i32_e32 v26, 0, v26
	v_mfma_f32_32x32x16_bf16 v[34:49], v[66:69], v[172:175], 0
	v_max_i32_e32 v27, 0, v27
	v_max_i32_e32 v20, 0, v20
	v_max_i32_e32 v21, 0, v21
	v_fma_f32 v18, v106, v18, 0
	v_fma_f32 v19, v107, v19, 0
	v_fma_f32 v26, v114, v26, 0
	v_fma_f32 v27, v115, v27, 0
	v_max_i32_e32 v28, 0, v28
	v_max_i32_e32 v29, 0, v29
	v_max_i32_e32 v22, 0, v22
	v_mfma_f32_32x32x16_bf16 v[34:49], v[70:73], v[2:5], v[34:49]
	v_max_i32_e32 v23, 0, v23
	v_max_i32_e32 v30, 0, v30
	v_max_i32_e32 v31, 0, v31
	v_fma_f32 v18, v108, v20, v18
	v_fma_f32 v19, v109, v21, v19
	v_fma_f32 v20, v116, v28, v26
	v_fma_f32 v21, v117, v29, v27
	v_max_i32_e32 v24, 0, v24
	v_max_i32_e32 v25, 0, v25
	v_max_i32_e32 v26, 0, v32
	v_mfma_f32_32x32x16_bf16 v[34:49], v[74:77], v[6:9], v[34:49]
	v_max_i32_e32 v27, 0, v33
	v_fma_f32 v18, v110, v22, v18
	v_fma_f32 v19, v111, v23, v19
	v_fma_f32 v20, v118, v30, v20
	v_fma_f32 v21, v119, v31, v21
	v_fma_f32 v18, v112, v24, v18
	v_fma_f32 v19, v113, v25, v19
	v_fma_f32 v20, v120, v26, v20
	v_fma_f32 v21, v121, v27, v21
	v_add_f32_e32 v18, v18, v19
	v_add_f32_e32 v20, v20, v21
	ds_read_b128 v[172:175], v11 offset:64
	s_nop 0
	v_permlane32_swap_b32_e32 v18, v20
	v_mfma_f32_32x32x16_bf16 v[34:49], v[78:81], v[160:163], v[34:49]
	v_add_f32_e32 v18, v18, v20
	ds_write_b32 v180, v18 offset:37120
	s_cbranch_vccnz .Lmidskip_b
	s_bitcmp1_b32 s33, 0
	s_cselect_b32 s1, 0x4800, 0
	v_add_u32_e32 v254, s1, v148
	v_add_u32_e32 v255, v254, v150
	v_add_u32_e32 v254, v254, v149
	s_waitcnt vmcnt(1)
	ds_write_b128 v254, v[82:85]
	s_waitcnt vmcnt(0)
	ds_write_b128 v255, v[86:89]
	s_waitcnt lgkmcnt(0)
	s_barrier
.Lmidskip_b:
	s_waitcnt lgkmcnt(4)
	v_mfma_f32_32x32x16_bf16 v[2:17], v[50:53], v[164:167], 0
	s_nop 7
	v_max_i32_e32 v42, 0, v42
	v_max_i32_e32 v43, 0, v43
	v_max_i32_e32 v34, 0, v34
	v_max_i32_e32 v35, 0, v35
	v_max_i32_e32 v36, 0, v36
	v_max_i32_e32 v37, 0, v37
	v_fma_f32 v42, v130, v42, 0
	v_fma_f32 v43, v131, v43, 0
	v_fma_f32 v34, v122, v34, 0
	v_fma_f32 v35, v123, v35, 0
	v_max_i32_e32 v18, 0, v44
	v_max_i32_e32 v19, 0, v45
	v_fma_f32 v20, v124, v36, v34
	v_fma_f32 v21, v125, v37, v35
	v_fma_f32 v18, v132, v18, v42
	v_fma_f32 v19, v133, v19, v43
	v_max_i32_e32 v22, 0, v38
	v_max_i32_e32 v23, 0, v39
	v_max_i32_e32 v24, 0, v46
	v_max_i32_e32 v25, 0, v47
	v_fma_f32 v20, v126, v22, v20
	v_fma_f32 v21, v127, v23, v21
	v_fma_f32 v18, v134, v24, v18
	v_fma_f32 v19, v135, v25, v19
	v_max_i32_e32 v22, 0, v40
	v_max_i32_e32 v23, 0, v41
	v_max_i32_e32 v24, 0, v48
	v_max_i32_e32 v25, 0, v49
	v_fma_f32 v20, v128, v22, v20
	v_fma_f32 v21, v129, v23, v21
	v_fma_f32 v18, v136, v24, v18
	v_fma_f32 v19, v137, v25, v19
	s_waitcnt lgkmcnt(3)
	v_mfma_f32_32x32x16_bf16 v[2:17], v[54:57], v[168:171], v[2:17]
	v_add_f32_e64 v34, v20, v21
	v_add_f32_e64 v35, v21, v20
	v_add_f32_e64 v36, v18, v19
	v_add_f32_e64 v37, v19, v18
	s_nop 0
	v_permlane32_swap_b32_e32 v34, v36
	v_add_f32_e32 v34, v34, v36
	v_mfma_f32_32x32x16_bf16 v[238:253], v[66:69], v[164:167], 0
	ds_write_b32 v180, v34 offset:38176
	s_waitcnt lgkmcnt(2)
	v_mfma_f32_32x32x16_bf16 v[2:17], v[58:61], v[172:175], v[2:17]
	v_mfma_f32_32x32x16_bf16 v[238:253], v[70:73], v[168:171], v[238:253]
	v_mfma_f32_32x32x16_bf16 v[2:17], v[62:65], v[176:179], v[2:17]
	v_mfma_f32_32x32x16_bf16 v[238:253], v[74:77], v[172:175], v[238:253]
	s_nop 10
	v_max_i32_e32 v2, 0, v2
	v_max_i32_e32 v3, 0, v3
	v_max_i32_e32 v10, 0, v10
	v_max_i32_e32 v11, 0, v11
	v_fma_f32 v2, v106, v2, 0
	v_fma_f32 v3, v107, v3, 0
	v_fma_f32 v10, v114, v10, 0
	v_fma_f32 v11, v115, v11, 0
	v_max_i32_e32 v4, 0, v4
	v_mfma_f32_32x32x16_bf16 v[238:253], v[78:81], v[176:179], v[238:253]
	v_max_i32_e32 v5, 0, v5
	v_max_i32_e32 v12, 0, v12
	v_max_i32_e32 v13, 0, v13
	v_fma_f32 v2, v108, v4, v2
	v_fma_f32 v3, v109, v5, v3
	v_fma_f32 v4, v116, v12, v10
	v_fma_f32 v5, v117, v13, v11
	v_max_i32_e32 v6, 0, v6
	v_max_i32_e32 v7, 0, v7
	v_max_i32_e32 v10, 0, v14
	v_max_i32_e32 v11, 0, v15
	v_fma_f32 v2, v110, v6, v2
	v_fma_f32 v3, v111, v7, v3
	v_fma_f32 v4, v118, v10, v4
	v_fma_f32 v5, v119, v11, v5
	v_max_i32_e32 v6, 0, v8
	v_max_i32_e32 v7, 0, v9
	v_max_i32_e32 v8, 0, v16
	v_max_i32_e32 v9, 0, v17
	v_fma_f32 v2, v112, v6, v2
	v_fma_f32 v3, v113, v7, v3
	v_fma_f32 v4, v120, v8, v4
	v_fma_f32 v5, v121, v9, v5
	v_add_f32_e32 v2, v2, v3
	v_add_f32_e32 v4, v4, v5
	v_max_i32_e32 v3, 0, v239
	s_nop 0
	v_permlane32_swap_b32_e32 v2, v4
	v_add_f32_e32 v2, v2, v4
	ds_write_b32 v180, v2 offset:37248
	v_max_i32_e32 v2, 0, v238
	v_max_i32_e32 v4, 0, v246
	v_max_i32_e32 v5, 0, v247
	v_fma_f32 v2, v122, v2, 0
	v_fma_f32 v3, v123, v3, 0
	v_fma_f32 v4, v130, v4, 0
	v_fma_f32 v5, v131, v5, 0
	v_max_i32_e32 v6, 0, v240
	v_max_i32_e32 v7, 0, v241
	v_max_i32_e32 v8, 0, v248
	v_max_i32_e32 v9, 0, v249
	v_fma_f32 v2, v124, v6, v2
	v_fma_f32 v3, v125, v7, v3
	v_fma_f32 v4, v132, v8, v4
	v_fma_f32 v5, v133, v9, v5
	v_max_i32_e32 v6, 0, v242
	v_max_i32_e32 v7, 0, v243
	v_max_i32_e32 v8, 0, v250
	v_max_i32_e32 v9, 0, v251
	v_fma_f32 v2, v126, v6, v2
	v_fma_f32 v3, v127, v7, v3
	v_fma_f32 v4, v134, v8, v4
	v_fma_f32 v5, v135, v9, v5
	v_max_i32_e32 v6, 0, v244
	v_max_i32_e32 v7, 0, v245
	v_max_i32_e32 v8, 0, v252
	v_max_i32_e32 v9, 0, v253
	v_fma_f32 v2, v128, v6, v2
	v_fma_f32 v3, v129, v7, v3
	v_fma_f32 v4, v136, v8, v4
	v_fma_f32 v5, v137, v9, v5
	v_add_f32_e32 v2, v2, v3
	v_add_f32_e32 v4, v4, v5
	s_nop 1
	v_permlane32_swap_b32_e32 v2, v4
	v_add_f32_e32 v2, v2, v4
	ds_write_b32 v180, v2 offset:38304
	s_branch .LBB0_439

	.amdhsa_kernel _Z10fwd_kernel4Args
		.amdhsa_group_segment_fixed_size 0
		.amdhsa_private_segment_fixed_size 0
		.amdhsa_kernarg_size 464
		.amdhsa_user_sgpr_count 2
		.amdhsa_user_sgpr_dispatch_ptr 0
		.amdhsa_user_sgpr_queue_ptr 0
		.amdhsa_user_sgpr_kernarg_segment_ptr 1
		.amdhsa_user_sgpr_dispatch_id 0
		.amdhsa_user_sgpr_kernarg_preload_length 0
		.amdhsa_user_sgpr_kernarg_preload_offset 0
		.amdhsa_user_sgpr_private_segment_size 0
		.amdhsa_uses_dynamic_stack 0
		.amdhsa_enable_private_segment 0
		.amdhsa_system_sgpr_workgroup_id_x 1
		.amdhsa_system_sgpr_workgroup_id_y 0
		.amdhsa_system_sgpr_workgroup_id_z 0
		.amdhsa_system_sgpr_workgroup_info 0
		.amdhsa_system_vgpr_workitem_id 0
		.amdhsa_next_free_vgpr 256
		.amdhsa_next_free_sgpr 100
		.amdhsa_accum_offset 256
		.amdhsa_reserve_vcc 1
		.amdhsa_float_round_mode_32 0
		.amdhsa_float_round_mode_16_64 0
		.amdhsa_float_denorm_mode_32 3
		.amdhsa_float_denorm_mode_16_64 3
		.amdhsa_dx10_clamp 1
		.amdhsa_ieee_mode 1
		.amdhsa_fp16_overflow 0
		.amdhsa_tg_split 0
		.amdhsa_exception_fp_ieee_invalid_op 0
		.amdhsa_exception_fp_denorm_src 0
		.amdhsa_exception_fp_ieee_div_zero 0
		.amdhsa_exception_fp_ieee_overflow 0
		.amdhsa_exception_fp_ieee_underflow 0
		.amdhsa_exception_fp_ieee_inexact 0
		.amdhsa_exception_int_div_zero 0
	.end_amdhsa_kernel

.Lfunc_end0:
	.size	_Z10fwd_kernel4Args, .Lfunc_end0-_Z10fwd_kernel4Args
	.set _Z10fwd_kernel4Args.num_vgpr, 256
	.set _Z10fwd_kernel4Args.num_agpr, 0
	.set _Z10fwd_kernel4Args.numbered_sgpr, 100
	.set _Z10fwd_kernel4Args.num_named_barrier, 0
	.set _Z10fwd_kernel4Args.private_seg_size, 0
	.set _Z10fwd_kernel4Args.uses_vcc, 1
	.set _Z10fwd_kernel4Args.uses_flat_scratch, 0
	.set _Z10fwd_kernel4Args.has_dyn_sized_stack, 0
	.set _Z10fwd_kernel4Args.has_recursion, 0
	.set _Z10fwd_kernel4Args.has_indirect_call, 0

amdhsa.kernels:
  - .agpr_count:     0
    .args:
      - .offset:         0
        .size:           208
        .value_kind:     by_value
      - .offset:         208
        .size:           4
        .value_kind:     hidden_block_count_x
      - .offset:         212
        .size:           4
        .value_kind:     hidden_block_count_y
      - .offset:         216
        .size:           4
        .value_kind:     hidden_block_count_z
      - .offset:         220
        .size:           2
        .value_kind:     hidden_group_size_x
      - .offset:         222
        .size:           2
        .value_kind:     hidden_group_size_y
      - .offset:         224
        .size:           2
        .value_kind:     hidden_group_size_z
      - .offset:         226
        .size:           2
        .value_kind:     hidden_remainder_x
      - .offset:         228
        .size:           2
        .value_kind:     hidden_remainder_y
      - .offset:         230
        .size:           2
        .value_kind:     hidden_remainder_z
      - .offset:         248
        .size:           8
        .value_kind:     hidden_global_offset_x
      - .offset:         256
        .size:           8
        .value_kind:     hidden_global_offset_y
      - .offset:         264
        .size:           8
        .value_kind:     hidden_global_offset_z
      - .offset:         272
        .size:           2
        .value_kind:     hidden_grid_dims
      - .offset:         328
        .size:           4
        .value_kind:     hidden_dynamic_lds_size
    .group_segment_fixed_size: 0
    .kernarg_segment_align: 8
    .kernarg_segment_size: 464
    .language:       OpenCL C
    .language_version:
      - 2
      - 0
    .max_flat_workgroup_size: 512
    .name:           _Z10fwd_kernel4Args
    .private_segment_fixed_size: 0
    .sgpr_count:     106
    .sgpr_spill_count: 51
    .symbol:         _Z10fwd_kernel4Args.kd
    .uniform_work_group_size: 1
    .uses_dynamic_stack: false
    .vgpr_count:     256
    .vgpr_spill_count: 0
    .wavefront_size: 64
